# adds phase 0: transposed bf16 weight stores use the nt cache policy
# baseline (speedup 1.0000x reference)
.LBB0_36:
	s_cmp_lt_i32 s92, 0
	s_cselect_b64 vcc, -1, 0
	s_ashr_i32 s9, s8, 31
	s_lshl_b64 s[8:9], s[8:9], 1
	s_add_u32 s4, s4, s8
	s_addc_u32 s5, s5, s9
	s_lshl_b32 s8, s92, 6
	s_and_b32 s8, s8, 0x7fffff80
	s_lshl_b32 s9, s92, 2
	ds_write2_b32 v153, v6, v7 offset1:1
	ds_write2_b32 v153, v8, v9 offset0:2 offset1:3
	v_add_u32_e32 v6, 0x410, v153
	ds_write2_b32 v6, v2, v3 offset1:1
	v_add_u32_e32 v2, 0x418, v153
	ds_write2_b32 v2, v4, v5 offset1:1
	v_add_u32_e32 v2, 0x820, v153
	ds_write2_b32 v2, v14, v15 offset1:1
	v_add_u32_e32 v2, 0x828, v153
	ds_write2_b32 v2, v16, v17 offset1:1
	v_add_u32_e32 v2, 0xc30, v153
	ds_write2_b32 v2, v10, v11 offset1:1
	v_add_u32_e32 v2, 0xc38, v153
	ds_write2_b32 v2, v12, v13 offset1:1
	v_add_u32_e32 v2, 0x1040, v153
	ds_write2_b32 v2, v22, v23 offset1:1
	v_add_u32_e32 v2, 0x1048, v153
	ds_write2_b32 v2, v24, v25 offset1:1
	v_add_u32_e32 v2, 0x1450, v153
	ds_write2_b32 v2, v18, v19 offset1:1
	v_add_u32_e32 v2, 0x1458, v153
	ds_write2_b32 v2, v20, v21 offset1:1
	v_add_u32_e32 v2, 0x1860, v153
	ds_write2_b32 v2, v30, v31 offset1:1
	v_add_u32_e32 v2, 0x1868, v153
	ds_write2_b32 v2, v32, v33 offset1:1
	v_add_u32_e32 v2, 0x1c70, v153
	ds_write2_b32 v2, v26, v27 offset1:1
	v_add_u32_e32 v2, 0x1c78, v153
	ds_write2_b32 v2, v28, v29 offset1:1
	v_add_u32_e32 v2, 0x2080, v153
	ds_write2_b32 v2, v38, v39 offset1:1
	v_add_u32_e32 v2, 0x2088, v153
	ds_write2_b32 v2, v40, v41 offset1:1
	v_add_u32_e32 v2, 0x2490, v153
	ds_write2_b32 v2, v34, v35 offset1:1
	v_add_u32_e32 v2, 0x2498, v153
	ds_write2_b32 v2, v36, v37 offset1:1
	v_add_u32_e32 v2, 0x28a0, v153
	ds_write2_b32 v2, v46, v47 offset1:1
	v_add_u32_e32 v2, 0x28a8, v153
	ds_write2_b32 v2, v48, v49 offset1:1
	v_add_u32_e32 v2, 0x2cb0, v153
	ds_write2_b32 v2, v42, v43 offset1:1
	v_add_u32_e32 v2, 0x2cb8, v153
	ds_write2_b32 v2, v44, v45 offset1:1
	v_add_u32_e32 v2, 0x30c0, v153
	ds_write2_b32 v2, v54, v55 offset1:1
	v_add_u32_e32 v2, 0x30c8, v153
	ds_write2_b32 v2, v56, v57 offset1:1
	v_add_u32_e32 v2, 0x34d0, v153
	ds_write2_b32 v2, v50, v51 offset1:1
	v_add_u32_e32 v2, 0x34d8, v153
	ds_write2_b32 v2, v52, v53 offset1:1
	v_add_u32_e32 v2, 0x38e0, v153
	ds_write2_b32 v2, v62, v63 offset1:1
	v_add_u32_e32 v2, 0x38e8, v153
	ds_write2_b32 v2, v64, v65 offset1:1
	v_add_u32_e32 v2, 0x3cf0, v153
	ds_write2_b32 v2, v58, v59 offset1:1
	v_add_u32_e32 v2, 0x3cf8, v153
	ds_write2_b32 v2, v60, v61 offset1:1
	s_waitcnt lgkmcnt(0)
	v_or_b32_e32 v2, s8, v142
	ds_read2_b32 v[8:9], v143 offset0:65 offset1:73
	ds_read2_b32 v[10:11], v143 offset1:8
	ds_read2_b32 v[12:13], v143 offset0:130 offset1:138
	ds_read2_b32 v[14:15], v143 offset0:195 offset1:203
	v_and_or_b32 v29, s9, 4, v2
	v_or_b32_e32 v30, v29, v144
	v_add_u32_e32 v28, 0x400, v143
	s_waitcnt lgkmcnt(2)
	v_cvt_pk_bf16_f32 v2, v10, v8
	v_cndmask_b32_e32 v8, v30, v140, vcc
	ds_read2_b32 v[16:17], v28 offset0:4 offset1:12
	ds_read2_b32 v[18:19], v28 offset0:69 offset1:77
	ds_read2_b32 v[20:21], v28 offset0:134 offset1:142
	ds_read2_b32 v[22:23], v28 offset0:199 offset1:207
	v_add_u32_e32 v8, s91, v8
	v_lshl_add_u64 v[6:7], s[4:5], 0, v[132:133]
	v_mad_u64_u32 v[24:25], s[4:5], v8, s60, 0
	v_ashrrev_i32_e32 v10, 31, v8
	v_mov_b32_e32 v8, v25
	v_mad_u64_u32 v[26:27], s[4:5], v10, s60, v[8:9]
	v_or_b32_e32 v8, v29, v145
	v_mov_b32_e32 v25, v26
	v_cndmask_b32_e32 v8, v8, v137, vcc
	s_waitcnt lgkmcnt(4)
	v_cvt_pk_bf16_f32 v3, v12, v14
	s_waitcnt lgkmcnt(2)
	v_cvt_pk_bf16_f32 v4, v16, v18
	s_waitcnt lgkmcnt(0)
	v_cvt_pk_bf16_f32 v5, v20, v22
	v_lshl_add_u64 v[24:25], v[24:25], 1, v[6:7]
	v_add_u32_e32 v8, s91, v8
	global_store_dwordx4 v[24:25], v[2:5], off nt
	s_waitcnt vmcnt(8)
	v_mov_b64_e32 v[38:39], v[98:99]
	s_waitcnt vmcnt(7)
	v_mov_b64_e32 v[34:35], v[102:103]
	v_cvt_pk_bf16_f32 v2, v11, v9
	v_ashrrev_i32_e32 v11, 31, v8
	v_mad_u64_u32 v[8:9], s[4:5], v8, s60, 0
	v_mov_b32_e32 v10, v9
	v_mad_u64_u32 v[10:11], s[4:5], v11, s60, v[10:11]
	v_mov_b32_e32 v9, v10
	v_cvt_pk_bf16_f32 v3, v13, v15
	v_cvt_pk_bf16_f32 v4, v17, v19
	v_cvt_pk_bf16_f32 v5, v21, v23
	v_lshl_add_u64 v[8:9], v[8:9], 1, v[6:7]
	ds_read2_b32 v[10:11], v143 offset0:16 offset1:24
	ds_read2_b32 v[12:13], v143 offset0:81 offset1:89
	ds_read2_b32 v[14:15], v143 offset0:146 offset1:154
	ds_read2_b32 v[16:17], v143 offset0:211 offset1:219
	ds_read2_b32 v[18:19], v28 offset0:20 offset1:28
	ds_read2_b32 v[20:21], v28 offset0:85 offset1:93
	ds_read2_b32 v[22:23], v28 offset0:150 offset1:158
	ds_read2_b32 v[24:25], v28 offset0:215 offset1:223
	global_store_dwordx4 v[8:9], v[2:5], off nt
	v_or_b32_e32 v8, 32, v30
	v_cndmask_b32_e32 v8, v8, v138, vcc
	v_add_u32_e32 v8, s91, v8
	s_waitcnt lgkmcnt(6)
	v_cvt_pk_bf16_f32 v2, v10, v12
	v_ashrrev_i32_e32 v12, 31, v8
	v_mad_u64_u32 v[8:9], s[4:5], v8, s60, 0
	v_mov_b32_e32 v10, v9
	v_mad_u64_u32 v[26:27], s[4:5], v12, s60, v[10:11]
	v_mov_b32_e32 v9, v26
	s_waitcnt lgkmcnt(4)
	v_cvt_pk_bf16_f32 v3, v14, v16
	s_waitcnt lgkmcnt(2)
	v_cvt_pk_bf16_f32 v4, v18, v20
	s_waitcnt lgkmcnt(0)
	v_cvt_pk_bf16_f32 v5, v22, v24
	v_lshl_add_u64 v[8:9], v[8:9], 1, v[6:7]
	global_store_dwordx4 v[8:9], v[2:5], off nt
	v_or_b32_e32 v8, v29, v146
	v_cndmask_b32_e32 v8, v8, v139, vcc
	v_add_u32_e32 v8, s91, v8
	v_cvt_pk_bf16_f32 v2, v11, v13
	v_ashrrev_i32_e32 v11, 31, v8
	v_mad_u64_u32 v[8:9], s[4:5], v8, s60, 0
	v_mov_b32_e32 v10, v9
	v_mad_u64_u32 v[10:11], s[4:5], v11, s60, v[10:11]
	v_mov_b32_e32 v9, v10
	v_cvt_pk_bf16_f32 v3, v15, v17
	v_cvt_pk_bf16_f32 v4, v19, v21
	v_cvt_pk_bf16_f32 v5, v23, v25
	v_lshl_add_u64 v[8:9], v[8:9], 1, v[6:7]
	ds_read2_b32 v[10:11], v143 offset0:32 offset1:40
	ds_read2_b32 v[12:13], v143 offset0:97 offset1:105
	ds_read2_b32 v[14:15], v143 offset0:162 offset1:170
	ds_read2_b32 v[16:17], v143 offset0:227 offset1:235
	ds_read2_b32 v[18:19], v28 offset0:36 offset1:44
	ds_read2_b32 v[20:21], v28 offset0:101 offset1:109
	ds_read2_b32 v[22:23], v28 offset0:166 offset1:174
	ds_read2_b32 v[24:25], v28 offset0:231 offset1:239
	global_store_dwordx4 v[8:9], v[2:5], off nt
	v_or_b32_e32 v8, 64, v30
	v_cndmask_b32_e32 v8, v8, v147, vcc
	v_add_u32_e32 v8, s91, v8
	s_waitcnt lgkmcnt(6)
	v_cvt_pk_bf16_f32 v2, v10, v12
	v_ashrrev_i32_e32 v12, 31, v8
	v_mad_u64_u32 v[8:9], s[4:5], v8, s60, 0
	v_mov_b32_e32 v10, v9
	v_mad_u64_u32 v[26:27], s[4:5], v12, s60, v[10:11]
	v_mov_b32_e32 v9, v26
	s_waitcnt lgkmcnt(4)
	v_cvt_pk_bf16_f32 v3, v14, v16
	s_waitcnt lgkmcnt(2)
	v_cvt_pk_bf16_f32 v4, v18, v20
	s_waitcnt lgkmcnt(0)
	v_cvt_pk_bf16_f32 v5, v22, v24
	v_lshl_add_u64 v[8:9], v[8:9], 1, v[6:7]
	global_store_dwordx4 v[8:9], v[2:5], off nt
	v_or_b32_e32 v8, v29, v149
	v_cndmask_b32_e32 v8, v8, v148, vcc
	v_add_u32_e32 v8, s91, v8
	v_cvt_pk_bf16_f32 v2, v11, v13
	v_ashrrev_i32_e32 v11, 31, v8
	v_mad_u64_u32 v[8:9], s[4:5], v8, s60, 0
	v_mov_b32_e32 v10, v9
	v_mad_u64_u32 v[10:11], s[4:5], v11, s60, v[10:11]
	v_mov_b32_e32 v9, v10
	v_cvt_pk_bf16_f32 v3, v15, v17
	v_cvt_pk_bf16_f32 v4, v19, v21
	v_cvt_pk_bf16_f32 v5, v23, v25
	v_lshl_add_u64 v[8:9], v[8:9], 1, v[6:7]
	ds_read2_b32 v[10:11], v143 offset0:48 offset1:56
	ds_read2_b32 v[12:13], v143 offset0:113 offset1:121
	ds_read2_b32 v[14:15], v143 offset0:178 offset1:186
	ds_read2_b32 v[16:17], v143 offset0:243 offset1:251
	ds_read2_b32 v[18:19], v28 offset0:52 offset1:60
	ds_read2_b32 v[20:21], v28 offset0:117 offset1:125
	ds_read2_b32 v[22:23], v28 offset0:182 offset1:190
	ds_read2_b32 v[24:25], v28 offset0:247 offset1:255
	global_store_dwordx4 v[8:9], v[2:5], off nt
	v_or_b32_e32 v8, 0x60, v30
	v_cndmask_b32_e32 v8, v8, v150, vcc
	v_add_u32_e32 v8, s91, v8
	s_waitcnt lgkmcnt(6)
	v_cvt_pk_bf16_f32 v2, v10, v12
	v_ashrrev_i32_e32 v12, 31, v8
	v_mad_u64_u32 v[8:9], s[4:5], v8, s60, 0
	v_mov_b32_e32 v10, v9
	v_mad_u64_u32 v[26:27], s[4:5], v12, s60, v[10:11]
	v_mov_b32_e32 v9, v26
	s_waitcnt lgkmcnt(4)
	v_cvt_pk_bf16_f32 v3, v14, v16
	s_waitcnt lgkmcnt(2)
	v_cvt_pk_bf16_f32 v4, v18, v20
	s_waitcnt lgkmcnt(0)
	v_cvt_pk_bf16_f32 v5, v22, v24
	v_lshl_add_u64 v[8:9], v[8:9], 1, v[6:7]
	global_store_dwordx4 v[8:9], v[2:5], off nt
	v_mov_b64_e32 v[30:31], v[90:91]
	s_waitcnt vmcnt(12)
	v_mov_b64_e32 v[46:47], v[106:107]
	v_or_b32_e32 v2, v29, v152
	v_cndmask_b32_e32 v8, v2, v151, vcc
	v_add_u32_e32 v8, s91, v8
	v_cvt_pk_bf16_f32 v2, v11, v13
	v_ashrrev_i32_e32 v11, 31, v8
	v_mad_u64_u32 v[8:9], s[4:5], v8, s60, 0
	v_mov_b32_e32 v10, v9
	v_mad_u64_u32 v[10:11], s[4:5], v11, s60, v[10:11]
	v_mov_b32_e32 v9, v10
	v_cvt_pk_bf16_f32 v3, v15, v17
	v_cvt_pk_bf16_f32 v4, v19, v21
	v_cvt_pk_bf16_f32 v5, v23, v25
	v_lshl_add_u64 v[6:7], v[8:9], 1, v[6:7]
	global_store_dwordx4 v[6:7], v[2:5], off nt
	s_waitcnt lgkmcnt(0)
	v_mov_b64_e32 v[6:7], v[66:67]
	v_mov_b64_e32 v[14:15], v[74:75]
	v_mov_b64_e32 v[2:3], v[70:71]
	v_mov_b64_e32 v[10:11], v[78:79]
	v_mov_b64_e32 v[22:23], v[82:83]
	v_mov_b64_e32 v[18:19], v[86:87]
	v_mov_b64_e32 v[26:27], v[94:95]
	s_waitcnt vmcnt(12)
	v_mov_b64_e32 v[42:43], v[110:111]
	s_waitcnt vmcnt(11)
	v_mov_b64_e32 v[54:55], v[114:115]
	s_waitcnt vmcnt(10)
	v_mov_b64_e32 v[50:51], v[118:119]
	s_waitcnt vmcnt(9)
	v_mov_b64_e32 v[62:63], v[122:123]
	s_waitcnt vmcnt(8)
	v_mov_b64_e32 v[58:59], v[126:127]
	s_andn2_b64 vcc, exec, s[36:37]
	v_mov_b64_e32 v[8:9], v[68:69]
	v_mov_b64_e32 v[4:5], v[72:73]
	v_mov_b64_e32 v[16:17], v[76:77]
	v_mov_b64_e32 v[12:13], v[80:81]
	v_mov_b64_e32 v[24:25], v[84:85]
	v_mov_b64_e32 v[20:21], v[88:89]
	v_mov_b64_e32 v[32:33], v[92:93]
	v_mov_b64_e32 v[28:29], v[96:97]
	v_mov_b64_e32 v[40:41], v[100:101]
	v_mov_b64_e32 v[36:37], v[104:105]
	v_mov_b64_e32 v[48:49], v[108:109]
	v_mov_b64_e32 v[44:45], v[112:113]
	v_mov_b64_e32 v[56:57], v[116:117]
	v_mov_b64_e32 v[52:53], v[120:121]
	v_mov_b64_e32 v[64:65], v[124:125]
	v_mov_b64_e32 v[60:61], v[128:129]
	s_mov_b64 s[4:5], s[10:11]
	s_mov_b32 s92, s81
	s_mov_b32 s91, s80
	s_mov_b32 s8, s82
	s_mov_b32 s60, s63
	s_cbranch_vccnz .LBB0_62

.LBB0_64:
	s_waitcnt lgkmcnt(0)
	ds_read2_b32 v[4:5], v20 offset1:33
	ds_read2_b32 v[6:7], v20 offset0:66 offset1:99
	ds_read2_b32 v[8:9], v20 offset0:132 offset1:165
	ds_read2_b32 v[10:11], v20 offset0:198 offset1:231
	s_mul_i32 s1, s14, 0x3c00000
	s_mul_hi_i32 s0, s14, 0x3c00000
	s_add_u32 s1, s95, s1
	s_addc_u32 s4, s44, s0
	s_lshl_b32 s0, s62, 7
	s_and_b32 s0, s0, 0xf80
	s_add_u32 s0, s1, s0
	s_waitcnt lgkmcnt(3)
	v_cvt_pk_bf16_f32 v4, v4, v5
	s_waitcnt lgkmcnt(2)
	v_cvt_pk_bf16_f32 v5, v6, v7
	s_waitcnt lgkmcnt(0)
	v_cvt_pk_bf16_f32 v7, v10, v11
	ds_read2_b32 v[10:11], v21 offset1:33
	ds_read2_b32 v[14:15], v21 offset0:66 offset1:99
	ds_read2_b32 v[16:17], v21 offset0:132 offset1:165
	ds_read2_b32 v[34:35], v21 offset0:198 offset1:231
	s_addc_u32 s1, s4, 0
	v_lshl_add_u64 v[12:13], v[130:131], 1, s[0:1]
	v_add_lshl_u32 v2, s13, v18, 12
	v_cvt_pk_bf16_f32 v6, v8, v9
	v_lshl_add_u64 v[8:9], v[12:13], 0, v[2:3]
	global_store_dwordx4 v[8:9], v[4:7], off nt
	v_add_lshl_u32 v2, s13, v137, 12
	v_lshl_add_u64 v[8:9], v[12:13], 0, v[2:3]
	s_waitcnt lgkmcnt(3)
	v_cvt_pk_bf16_f32 v4, v10, v11
	s_waitcnt lgkmcnt(2)
	v_cvt_pk_bf16_f32 v5, v14, v15
	s_waitcnt lgkmcnt(1)
	v_cvt_pk_bf16_f32 v6, v16, v17
	s_waitcnt lgkmcnt(0)
	v_cvt_pk_bf16_f32 v7, v34, v35
	ds_read2_b32 v[10:11], v22 offset1:33
	ds_read2_b32 v[14:15], v22 offset0:66 offset1:99
	ds_read2_b32 v[16:17], v22 offset0:132 offset1:165
	ds_read2_b32 v[34:35], v22 offset0:198 offset1:231
	global_store_dwordx4 v[8:9], v[4:7], off nt
	v_add_lshl_u32 v2, s13, v138, 12
	v_lshl_add_u64 v[8:9], v[12:13], 0, v[2:3]
	s_waitcnt lgkmcnt(3)
	v_cvt_pk_bf16_f32 v4, v10, v11
	s_waitcnt lgkmcnt(2)
	v_cvt_pk_bf16_f32 v5, v14, v15
	s_waitcnt lgkmcnt(1)
	v_cvt_pk_bf16_f32 v6, v16, v17
	s_waitcnt lgkmcnt(0)
	v_cvt_pk_bf16_f32 v7, v34, v35
	ds_read2_b32 v[10:11], v23 offset1:33
	ds_read2_b32 v[14:15], v23 offset0:66 offset1:99
	ds_read2_b32 v[16:17], v23 offset0:132 offset1:165
	ds_read2_b32 v[34:35], v23 offset0:198 offset1:231
	v_add_lshl_u32 v2, s13, v139, 12
	global_store_dwordx4 v[8:9], v[4:7], off nt
	v_lshl_add_u64 v[8:9], v[12:13], 0, v[2:3]
	s_waitcnt lgkmcnt(3)
	v_cvt_pk_bf16_f32 v4, v10, v11
	s_waitcnt lgkmcnt(2)
	v_cvt_pk_bf16_f32 v5, v14, v15
	s_waitcnt lgkmcnt(1)
	v_cvt_pk_bf16_f32 v6, v16, v17
	s_waitcnt lgkmcnt(0)
	v_cvt_pk_bf16_f32 v7, v34, v35
	global_store_dwordx4 v[8:9], v[4:7], off nt
	s_waitcnt lgkmcnt(0)
